# baseline (speedup 1.0000x reference)
.LBB1_18:
	s_setprio 0
	v_log_f32_e32 v66, v50
	v_rcp_f32_e32 v50, v50
	v_lshl_add_u32 v1, v1, 6, v220
	v_sub_f32_e32 v2, v66, v2
	v_log_f32_e32 v66, v51
	v_rcp_f32_e32 v51, v51
	s_movk_i32 s4, 0x104
	v_mul_lo_u32 v1, v1, s4
	v_lshl_add_u32 v1, v219, 4, v1
	v_sub_f32_e32 v3, v66, v3
	s_barrier
	v_mul_f32_e32 v50, v50, v216
	v_add_u32_e32 v67, 0x2080, v1
	ds_write2_b32 v1, v2, v3 offset1:1
	v_log_f32_e32 v2, v52
	v_mul_f32_e32 v3, v51, v217
	v_rcp_f32_e32 v51, v52
	ds_write2_b32 v67, v50, v3 offset1:1
	v_log_f32_e32 v3, v53
	v_sub_f32_e32 v2, v2, v4
	v_mul_f32_e32 v4, v51, v214
	v_rcp_f32_e32 v51, v53
	v_sub_f32_e32 v3, v3, v5
	ds_write2_b32 v1, v2, v3 offset0:2 offset1:3
	v_log_f32_e32 v2, v54
	v_add_u32_e32 v50, 0x2088, v1
	v_mul_f32_e32 v3, v51, v215
	ds_write2_b32 v50, v4, v3 offset1:1
	v_log_f32_e32 v3, v55
	v_sub_f32_e32 v2, v2, v6
	v_rcp_f32_e32 v6, v55
	v_rcp_f32_e32 v5, v54
	v_sub_f32_e32 v3, v3, v7
	ds_write2_b32 v1, v2, v3 offset0:8 offset1:9
	v_mul_f32_e32 v3, v6, v213
	v_rcp_f32_e32 v6, v56
	v_mul_f32_e32 v4, v5, v212
	v_add_u32_e32 v5, 0x20a0, v1
	v_log_f32_e32 v2, v56
	ds_write2_b32 v5, v4, v3 offset1:1
	v_log_f32_e32 v3, v57
	v_mul_f32_e32 v4, v6, v210
	v_rcp_f32_e32 v6, v57
	v_sub_f32_e32 v2, v2, v8
	v_sub_f32_e32 v3, v3, v9
	ds_write2_b32 v1, v2, v3 offset0:10 offset1:11
	v_mul_f32_e32 v3, v6, v211
	v_rcp_f32_e32 v6, v58
	v_add_u32_e32 v5, 0x20a8, v1
	v_log_f32_e32 v2, v58
	ds_write2_b32 v5, v4, v3 offset1:1
	v_log_f32_e32 v3, v59
	v_mul_f32_e32 v4, v6, v208
	v_rcp_f32_e32 v6, v59
	v_sub_f32_e32 v2, v2, v10
	v_sub_f32_e32 v3, v3, v11
	ds_write2_b32 v1, v2, v3 offset0:16 offset1:17
	v_mul_f32_e32 v3, v6, v209
	v_rcp_f32_e32 v6, v60
	v_add_u32_e32 v5, 0x20c0, v1
	v_log_f32_e32 v2, v60
	ds_write2_b32 v5, v4, v3 offset1:1
	v_log_f32_e32 v3, v61
	v_mul_f32_e32 v4, v6, v204
	v_rcp_f32_e32 v6, v61
	v_sub_f32_e32 v2, v2, v12
	v_sub_f32_e32 v3, v3, v13
	ds_write2_b32 v1, v2, v3 offset0:18 offset1:19
	v_mul_f32_e32 v3, v6, v205
	v_rcp_f32_e32 v6, v62
	v_add_u32_e32 v5, 0x20c8, v1
	v_log_f32_e32 v2, v62
	ds_write2_b32 v5, v4, v3 offset1:1
	v_log_f32_e32 v3, v63
	v_mul_f32_e32 v4, v6, v202
	v_rcp_f32_e32 v6, v63
	v_sub_f32_e32 v2, v2, v14
	v_sub_f32_e32 v3, v3, v15
	ds_write2_b32 v1, v2, v3 offset0:24 offset1:25
	v_mul_f32_e32 v3, v6, v203
	v_rcp_f32_e32 v6, v64
	v_add_u32_e32 v5, 0x20e0, v1
	v_log_f32_e32 v2, v64
	ds_write2_b32 v5, v4, v3 offset1:1
	v_log_f32_e32 v3, v65
	v_mul_f32_e32 v4, v6, v196
	v_rcp_f32_e32 v6, v65
	v_sub_f32_e32 v2, v2, v16
	v_sub_f32_e32 v3, v3, v17
	ds_write2_b32 v1, v2, v3 offset0:26 offset1:27
	v_mul_f32_e32 v3, v6, v197
	v_rcp_f32_e32 v6, v18
	v_add_u32_e32 v5, 0x20e8, v1
	v_log_f32_e32 v2, v18
	ds_write2_b32 v5, v4, v3 offset1:1
	v_log_f32_e32 v3, v19
	v_mul_f32_e32 v4, v6, v206
	v_rcp_f32_e32 v6, v19
	v_sub_f32_e32 v2, v2, v34
	v_sub_f32_e32 v3, v3, v35
	ds_write2_b32 v1, v2, v3 offset0:32 offset1:33
	v_mul_f32_e32 v3, v6, v207
	v_rcp_f32_e32 v6, v20
	v_add_u32_e32 v5, 0x2100, v1
	v_log_f32_e32 v2, v20
	ds_write2_b32 v5, v4, v3 offset1:1
	v_log_f32_e32 v3, v21
	v_mul_f32_e32 v4, v6, v200
	v_rcp_f32_e32 v6, v21
	v_sub_f32_e32 v2, v2, v36
	v_sub_f32_e32 v3, v3, v37
	ds_write2_b32 v1, v2, v3 offset0:34 offset1:35
	v_mul_f32_e32 v3, v6, v201
	v_rcp_f32_e32 v6, v22
	v_add_u32_e32 v5, 0x2108, v1
	v_log_f32_e32 v2, v22
	ds_write2_b32 v5, v4, v3 offset1:1
	v_log_f32_e32 v3, v23
	v_mul_f32_e32 v4, v6, v198
	v_rcp_f32_e32 v6, v23
	v_sub_f32_e32 v2, v2, v38
	v_sub_f32_e32 v3, v3, v39
	ds_write2_b32 v1, v2, v3 offset0:40 offset1:41
	v_mul_f32_e32 v3, v6, v199
	v_rcp_f32_e32 v6, v24
	v_add_u32_e32 v5, 0x2120, v1
	v_log_f32_e32 v2, v24
	ds_write2_b32 v5, v4, v3 offset1:1
	v_log_f32_e32 v3, v25
	v_mul_f32_e32 v4, v6, v194
	v_rcp_f32_e32 v6, v25
	v_sub_f32_e32 v2, v2, v40
	v_sub_f32_e32 v3, v3, v41
	ds_write2_b32 v1, v2, v3 offset0:42 offset1:43
	v_mul_f32_e32 v3, v6, v195
	v_rcp_f32_e32 v6, v26
	v_add_u32_e32 v5, 0x2128, v1
	v_log_f32_e32 v2, v26
	ds_write2_b32 v5, v4, v3 offset1:1
	v_log_f32_e32 v3, v27
	v_mul_f32_e32 v4, v6, v192
	v_rcp_f32_e32 v6, v27
	v_sub_f32_e32 v2, v2, v42
	v_sub_f32_e32 v3, v3, v43
	ds_write2_b32 v1, v2, v3 offset0:48 offset1:49
	v_mul_f32_e32 v3, v6, v193
	v_rcp_f32_e32 v6, v28
	v_add_u32_e32 v5, 0x2140, v1
	v_log_f32_e32 v2, v28
	ds_write2_b32 v5, v4, v3 offset1:1
	v_log_f32_e32 v3, v29
	v_mul_f32_e32 v4, v6, v190
	v_rcp_f32_e32 v6, v29
	v_sub_f32_e32 v2, v2, v44
	v_sub_f32_e32 v3, v3, v45
	ds_write2_b32 v1, v2, v3 offset0:50 offset1:51
	v_mul_f32_e32 v3, v6, v191
	v_rcp_f32_e32 v6, v30
	v_add_u32_e32 v5, 0x2148, v1
	v_log_f32_e32 v2, v30
	ds_write2_b32 v5, v4, v3 offset1:1
	v_log_f32_e32 v3, v31
	v_mul_f32_e32 v4, v6, v188
	v_rcp_f32_e32 v6, v31
	v_sub_f32_e32 v2, v2, v46
	v_sub_f32_e32 v3, v3, v47
	v_add_u32_e32 v5, 0x2160, v1
	ds_write2_b32 v1, v2, v3 offset0:56 offset1:57
	v_mul_f32_e32 v3, v6, v189
	v_log_f32_e32 v2, v32
	ds_write2_b32 v5, v4, v3 offset1:1
	v_log_f32_e32 v3, v33
	v_rcp_f32_e32 v6, v32
	v_rcp_f32_e32 v5, v33
	v_sub_f32_e32 v2, v2, v48
	v_sub_f32_e32 v3, v3, v49
	s_ashr_i32 s3, s2, 31
	v_mul_f32_e32 v4, v6, v186
	v_add_u32_e32 v6, 0x2168, v1
	ds_write2_b32 v1, v2, v3 offset0:58 offset1:59
	v_mul_f32_e32 v1, v5, v187
	s_lshl_b64 s[2:3], s[2:3], 14
	ds_write2_b32 v6, v4, v1 offset1:1
	v_and_b32_e32 v1, 63, v0
	s_add_u32 s0, s0, s2
	v_lshlrev_b32_e32 v2, 2, v1
	v_ashrrev_i32_e32 v1, 31, v0
	s_addc_u32 s1, s1, s3
	v_lshl_add_u64 v[4:5], v[0:1], 2, s[0:1]
	s_mov_b32 s2, 0
	s_mov_b64 s[0:1], 0x800
	s_waitcnt lgkmcnt(0)
	s_barrier
